# cmp pass 2: second group's boundary exps and bpermutes issued together with the first group's, so only one LDS round trip is exposed per item
# baseline (speedup 1.0000x reference)
; #define LAS __attribute__((address_space(3)))
; __device__ __forceinline__ unsigned lds_addr(const LAS void* p) { return (unsigned)(size_t)p; }
; __device__ __forceinline__ void imp_accum(const f32x4 (&s)[4], float& carry, LAS float* impt  , int jb, int c, int q4, int lane) {
;     float rot[4];
; #pragma unroll
;     for (int T_ = 0; T_ < 4; ++T_) rot[T_] = __shfl(s[T_][3], (lane + 48) & 63);
; #pragma unroll
;     for (int T_ = 0; T_ < 4; ++T_) { const float prev = (q4 == 0) ? (T_ == 0 ? carry : rot[T_ == 0 ? 0 : T_ - 1]) : rot[T_];
;         float v = (s[T_][0] + s[T_][1]) + (s[T_][2] + s[T_][3]) + prev;
;         v += __builtin_bit_cast(float, __builtin_amdgcn_mov_dpp(__builtin_bit_cast(int, v), 0xB1, 0xF, 0xF, true));
;         v += __builtin_bit_cast(float, __builtin_amdgcn_mov_dpp(__builtin_bit_cast(int, v), 0x4E, 0xF, 0xF, true));
;         if ((c & 3) == 0) impt[jb + 4 * T_ + q4] = v; }
;     carry = rot[3];
; }
; __device__ __forceinline__ void cmp_phase(Frame& F) {
;     ...
; #pragma unroll
;                 for (int T_ = 0; T_ < 4; ++T_)
; #pragma unroll
;                     for (int q = 0; q < 4; ++q) { s0[T_][q] = __builtin_amdgcn_exp2f(s0[T_][q]); s1[T_][q] = __builtin_amdgcn_exp2f(s1[T_][q]); }
;                 imp_accum(s0, carry0, impA, kt * 16, c, kq, lane); imp_accum(s1, carry1, impB, kt * 16, c, kq, lane);
;                 pv_tile<2>(g0, g1, s0, s1, lds_addr(sb + K8TB) + vlane);
.LBB0_1585:
	s_and_b64 vcc, exec, s[22:23]
	s_cbranch_vccz .LBB0_1570
	v_exp_f32_e32 v138, v109
	v_exp_f32_e32 v109, v110
	v_exp_f32_e32 v110, v111
	v_exp_f32_e32 v134, v108
	v_exp_f32_e32 v108, v107
	v_exp_f32_e32 v107, v103
	v_exp_f32_e32 v103, v99
	ds_bpermute_b32 v146, v183, v110
	ds_bpermute_b32 v145, v183, v108
	ds_bpermute_b32 v144, v183, v107
	ds_bpermute_b32 v99, v183, v103
	v_exp_f32_e32 v91, v91
	v_exp_f32_e32 v231, v88
	v_exp_f32_e32 v232, v89
	v_exp_f32_e32 v89, v87
	v_exp_f32_e32 v88, v83
	v_exp_f32_e32 v87, v95
	ds_bpermute_b32 v228, v183, v91
	v_exp_f32_e32 v90, v90
	ds_bpermute_b32 v229, v183, v89
	ds_bpermute_b32 v230, v183, v88
	ds_bpermute_b32 v83, v183, v87
	v_add_f32_e32 v147, v134, v138
	v_add_f32_e32 v148, v109, v110
	s_waitcnt lgkmcnt(4)
	v_cndmask_b32_e64 v196, v146, v193, s[2:3]
	v_add_f32_e32 v147, v147, v148
	v_add_f32_e32 v196, v147, v196
	s_add_i32 s22, s79, s48
	v_add_u32_e32 v111, s22, v117
	v_exp_f32_e32 v140, v104
	v_exp_f32_e32 v105, v105
	v_exp_f32_e32 v104, v106
	v_cndmask_b32_e64 v197, v145, v146, s[2:3]
	v_add_f32_e32 v146, v140, v105
	v_add_f32_e32 v147, v104, v108
	v_add_f32_e32 v146, v146, v147
	v_add_f32_e32 v197, v146, v197
	v_exp_f32_e32 v106, v100
	v_exp_f32_e32 v101, v101
	v_exp_f32_e32 v100, v102
	v_cndmask_b32_e64 v198, v144, v145, s[2:3]
	v_add_f32_e32 v145, v106, v101
	v_add_f32_e32 v146, v100, v107
	v_add_f32_e32 v145, v145, v146
	v_add_f32_e32 v198, v145, v198
	v_exp_f32_e32 v102, v96
	v_exp_f32_e32 v97, v97
	v_exp_f32_e32 v96, v98
	v_cndmask_b32_e64 v199, v99, v144, s[2:3]
	v_add_f32_e32 v144, v102, v97
	v_add_f32_e32 v145, v96, v103
	v_add_f32_e32 v144, v144, v145
	v_add_f32_e32 v199, v144, v199
	v_add_f32_e32 v148, v231, v232
	v_add_f32_e32 v149, v90, v91
	s_waitcnt lgkmcnt(0)
	v_cndmask_b32_e64 v200, v228, v192, s[2:3]
	v_add_f32_e32 v148, v148, v149
	v_add_f32_e32 v200, v148, v200
	v_exp_f32_e32 v95, v84
	v_exp_f32_e32 v85, v85
	v_exp_f32_e32 v84, v86
	v_cndmask_b32_e64 v201, v229, v228, s[2:3]
	v_add_f32_e32 v147, v95, v85
	v_add_f32_e32 v148, v84, v89
	v_add_f32_e32 v147, v147, v148
	v_add_f32_e32 v201, v147, v201
	v_exp_f32_e32 v86, v80
	v_exp_f32_e32 v81, v81
	v_exp_f32_e32 v80, v82
	v_cndmask_b32_e64 v202, v230, v229, s[2:3]
	v_add_f32_e32 v146, v86, v81
	v_add_f32_e32 v147, v80, v88
	v_add_f32_e32 v146, v146, v147
	v_add_f32_e32 v202, v146, v202
	v_exp_f32_e32 v92, v92
	v_exp_f32_e32 v93, v93
	v_exp_f32_e32 v82, v94
	v_cndmask_b32_e64 v203, v83, v230, s[2:3]
	v_add_f32_e32 v145, v92, v93
	v_add_f32_e32 v146, v82, v87
	v_add_f32_e32 v145, v145, v146
	v_add_f32_e32 v203, v145, v203
	v_add_f32_dpp v196, v196, v196 quad_perm:[1,0,3,2] row_mask:0xf bank_mask:0xf bound_ctrl:1
	v_add_f32_dpp v197, v197, v197 quad_perm:[1,0,3,2] row_mask:0xf bank_mask:0xf bound_ctrl:1
	v_add_f32_dpp v198, v198, v198 quad_perm:[1,0,3,2] row_mask:0xf bank_mask:0xf bound_ctrl:1
	v_add_f32_dpp v199, v199, v199 quad_perm:[1,0,3,2] row_mask:0xf bank_mask:0xf bound_ctrl:1
	v_add_f32_dpp v200, v200, v200 quad_perm:[1,0,3,2] row_mask:0xf bank_mask:0xf bound_ctrl:1
	v_add_f32_dpp v201, v201, v201 quad_perm:[1,0,3,2] row_mask:0xf bank_mask:0xf bound_ctrl:1
	v_add_f32_dpp v202, v202, v202 quad_perm:[1,0,3,2] row_mask:0xf bank_mask:0xf bound_ctrl:1
	v_add_f32_dpp v203, v203, v203 quad_perm:[1,0,3,2] row_mask:0xf bank_mask:0xf bound_ctrl:1
	v_add_f32_dpp v196, v196, v196 quad_perm:[2,3,0,1] row_mask:0xf bank_mask:0xf bound_ctrl:1
	v_add_f32_dpp v197, v197, v197 quad_perm:[2,3,0,1] row_mask:0xf bank_mask:0xf bound_ctrl:1
	v_add_f32_dpp v198, v198, v198 quad_perm:[2,3,0,1] row_mask:0xf bank_mask:0xf bound_ctrl:1
	v_add_f32_dpp v199, v199, v199 quad_perm:[2,3,0,1] row_mask:0xf bank_mask:0xf bound_ctrl:1
	v_add_f32_dpp v200, v200, v200 quad_perm:[2,3,0,1] row_mask:0xf bank_mask:0xf bound_ctrl:1
	v_add_f32_dpp v201, v201, v201 quad_perm:[2,3,0,1] row_mask:0xf bank_mask:0xf bound_ctrl:1
	v_add_f32_dpp v202, v202, v202 quad_perm:[2,3,0,1] row_mask:0xf bank_mask:0xf bound_ctrl:1
	v_add_f32_dpp v203, v203, v203 quad_perm:[2,3,0,1] row_mask:0xf bank_mask:0xf bound_ctrl:1
	s_and_saveexec_b64 s[22:23], s[4:5]
	v_add_u32_e32 v212, 0x117c1, v111
	ds_write_b32 v212, v196
	ds_write_b32 v212, v197 offset:16
	ds_write_b32 v212, v198 offset:32
	ds_write_b32 v212, v199 offset:48
	ds_write_b32 v212, v200 offset:4096
	ds_write_b32 v212, v201 offset:4112
	ds_write_b32 v212, v202 offset:4128
	ds_write_b32 v212, v203 offset:4144
	s_or_b64 exec, exec, s[22:23]
	s_addk_i32 s37, 0x2400
	v_add_u32_e32 v145, s37, v173
	v_cvt_pk_bf16_f32 v146, v134, v138
	v_cvt_pk_bf16_f32 v147, v109, v110
	v_cvt_pk_bf16_f32 v148, v140, v105
	v_cvt_pk_bf16_f32 v149, v104, v108
	v_cvt_pk_bf16_f32 v104, v106, v101
	v_cvt_pk_bf16_f32 v105, v100, v107
	v_cvt_pk_bf16_f32 v106, v102, v97
	v_cvt_pk_bf16_f32 v107, v96, v103
	v_cvt_pk_bf16_f32 v100, v231, v232
	v_cvt_pk_bf16_f32 v101, v90, v91
	v_cvt_pk_bf16_f32 v102, v95, v85
	v_cvt_pk_bf16_f32 v103, v84, v89
	v_cvt_pk_bf16_f32 v84, v86, v81
	v_cvt_pk_bf16_f32 v85, v80, v88
	v_cvt_pk_bf16_f32 v86, v92, v93
	v_cvt_pk_bf16_f32 v87, v82, v87
	ds_read_b64_tr_b16 v[88:89], v145 offset:0
	ds_read_b64_tr_b16 v[90:91], v145 offset:0x1200
	ds_read_b64_tr_b16 v[92:93], v145 offset:0x2400
	ds_read_b64_tr_b16 v[94:95], v145 offset:0x3600
	ds_read_b64_tr_b16 v[108:109], v145 offset:32
	ds_read_b64_tr_b16 v[110:111], v145 offset:0x1220
	ds_read_b64_tr_b16 v[150:151], v145 offset:0x2420
	ds_read_b64_tr_b16 v[152:153], v145 offset:0x3620
	ds_read_b64_tr_b16 v[154:155], v145 offset:64
	ds_read_b64_tr_b16 v[156:157], v145 offset:0x1240
	ds_read_b64_tr_b16 v[158:159], v145 offset:0x2440
	ds_read_b64_tr_b16 v[160:161], v145 offset:0x3640
	s_setprio 1
	s_waitcnt lgkmcnt(8)
; #define SBAR() __builtin_amdgcn_sched_barrier(0)
; __device__ __forceinline__ bf16x8 ppack(const f32x4 a, const f32x4 b) { const u32x4 w = pack8f(a, b); return __builtin_bit_cast(bf16x8, w); }
; #define PV_RD(dt) do { TRRD(r[dt][0], vb, (dt) * 32); TRRD(r[dt][1], vb, (dt) * 32 + 4608); TRRD(r[dt][2], vb, (dt) * 32 + 9216); TRRD(r[dt][3], vb, (dt) * 32 + 9216 + 4608); } while (0)
; #define PV_W(n) asm volatile("s_waitcnt lgkmcnt(" #n ")" ::: "memory"); SBAR()
; template <int NG, class G> __device__ __forceinline__ void pv_tile(G& g0, G& g1, const f32x4 (&s0)[4], const f32x4 (&s1)[4], unsigned vb) {
;     const bf16x8 pa0 = ppack(s0[0], s0[1]), pa1 = ppack(s0[2], s0[3]);
;     bf16x8 pb0 = pa0, pb1 = pa1; if (NG == 2) { pb0 = ppack(s1[0], s1[1]); pb1 = ppack(s1[2], s1[3]); }
;     s16x4 r[8][4];
;     ...
;     PV_RD(0); PV_RD(1); PV_RD(2);
;     __builtin_amdgcn_s_setprio(1);
;     PV_W(8); PV_MM(0); SBAR(); PV_RD(3);
;     PV_W(8); PV_MM(1); SBAR(); PV_RD(4);
;     PV_W(8); PV_MM(2); SBAR(); PV_RD(5);
;     PV_W(8); PV_MM(3); SBAR(); PV_RD(6);
;     PV_W(8); PV_MM(4); SBAR(); PV_RD(7);
;     PV_W(8); PV_MM(5); PV_W(4); PV_MM(6); PV_W(0); PV_MM(7);
;     __builtin_amdgcn_s_setprio(0);
; __device__ __forceinline__ void imp_accum(const f32x4 (&s)[4], float& carry, LAS float* impt  , int jb, int c, int q4, int lane) {
;     ...
;     carry = rot[3];
	v_mfma_f32_16x16x32_bf16 v[76:79], v[88:91], v[146:149], v[76:79]
	v_mfma_f32_16x16x32_bf16 v[44:47], v[88:91], v[100:103], v[44:47]
	v_mfma_f32_16x16x32_bf16 v[76:79], v[92:95], v[104:107], v[76:79]
	v_mfma_f32_16x16x32_bf16 v[44:47], v[92:95], v[84:87], v[44:47]
	ds_read_b64_tr_b16 v[88:89], v145 offset:0x60
	ds_read_b64_tr_b16 v[90:91], v145 offset:0x1260
	ds_read_b64_tr_b16 v[92:93], v145 offset:0x2460
	ds_read_b64_tr_b16 v[94:95], v145 offset:0x3660
	s_waitcnt lgkmcnt(8)
	v_mfma_f32_16x16x32_bf16 v[72:75], v[108:111], v[146:149], v[72:75]
	v_mfma_f32_16x16x32_bf16 v[40:43], v[108:111], v[100:103], v[40:43]
	v_mfma_f32_16x16x32_bf16 v[72:75], v[150:153], v[104:107], v[72:75]
	v_mfma_f32_16x16x32_bf16 v[40:43], v[150:153], v[84:87], v[40:43]
	ds_read_b64_tr_b16 v[108:109], v145 offset:0x80
	ds_read_b64_tr_b16 v[110:111], v145 offset:0x1280
	ds_read_b64_tr_b16 v[150:151], v145 offset:0x2480
	ds_read_b64_tr_b16 v[152:153], v145 offset:0x3680
	s_waitcnt lgkmcnt(8)
	v_mfma_f32_16x16x32_bf16 v[68:71], v[154:157], v[146:149], v[68:71]
	v_mfma_f32_16x16x32_bf16 v[36:39], v[154:157], v[100:103], v[36:39]
	v_mfma_f32_16x16x32_bf16 v[68:71], v[158:161], v[104:107], v[68:71]
	v_mfma_f32_16x16x32_bf16 v[36:39], v[158:161], v[84:87], v[36:39]
	ds_read_b64_tr_b16 v[154:155], v145 offset:0xa0
	ds_read_b64_tr_b16 v[156:157], v145 offset:0x12a0
	ds_read_b64_tr_b16 v[158:159], v145 offset:0x24a0
	ds_read_b64_tr_b16 v[160:161], v145 offset:0x36a0
	s_waitcnt lgkmcnt(8)
	v_mfma_f32_16x16x32_bf16 v[64:67], v[88:91], v[146:149], v[64:67]
	v_mfma_f32_16x16x32_bf16 v[32:35], v[88:91], v[100:103], v[32:35]
	v_mfma_f32_16x16x32_bf16 v[64:67], v[92:95], v[104:107], v[64:67]
	v_mfma_f32_16x16x32_bf16 v[32:35], v[92:95], v[84:87], v[32:35]
	ds_read_b64_tr_b16 v[88:89], v145 offset:0xc0
	ds_read_b64_tr_b16 v[90:91], v145 offset:0x12c0
	ds_read_b64_tr_b16 v[92:93], v145 offset:0x24c0
	ds_read_b64_tr_b16 v[94:95], v145 offset:0x36c0
	s_waitcnt lgkmcnt(8)
	v_mfma_f32_16x16x32_bf16 v[60:63], v[108:111], v[146:149], v[60:63]
	v_mfma_f32_16x16x32_bf16 v[28:31], v[108:111], v[100:103], v[28:31]
	v_mfma_f32_16x16x32_bf16 v[60:63], v[150:153], v[104:107], v[60:63]
	v_mfma_f32_16x16x32_bf16 v[28:31], v[150:153], v[84:87], v[28:31]
	ds_read_b64_tr_b16 v[108:109], v145 offset:0xe0
	ds_read_b64_tr_b16 v[110:111], v145 offset:0x12e0
	ds_read_b64_tr_b16 v[150:151], v145 offset:0x24e0
	ds_read_b64_tr_b16 v[152:153], v145 offset:0x36e0
	s_waitcnt lgkmcnt(8)
	v_mfma_f32_16x16x32_bf16 v[56:59], v[154:157], v[146:149], v[56:59]
	s_waitcnt lgkmcnt(4)
	v_mfma_f32_16x16x32_bf16 v[24:27], v[154:157], v[100:103], v[24:27]
	v_mfma_f32_16x16x32_bf16 v[56:59], v[158:161], v[104:107], v[56:59]
	v_mfma_f32_16x16x32_bf16 v[24:27], v[158:161], v[84:87], v[24:27]
	v_mfma_f32_16x16x32_bf16 v[52:55], v[88:91], v[146:149], v[52:55]
	s_waitcnt lgkmcnt(0)
	v_mfma_f32_16x16x32_bf16 v[20:23], v[88:91], v[100:103], v[20:23]
	v_mfma_f32_16x16x32_bf16 v[52:55], v[92:95], v[104:107], v[52:55]
	v_mfma_f32_16x16x32_bf16 v[20:23], v[92:95], v[84:87], v[20:23]
	v_mfma_f32_16x16x32_bf16 v[48:51], v[108:111], v[146:149], v[48:51]
	v_mfma_f32_16x16x32_bf16 v[16:19], v[108:111], v[100:103], v[16:19]
	v_mfma_f32_16x16x32_bf16 v[48:51], v[150:153], v[104:107], v[48:51]
	v_mfma_f32_16x16x32_bf16 v[16:19], v[150:153], v[84:87], v[16:19]
	s_setprio 0
	v_mov_b32_e32 v192, v83
	v_mov_b32_e32 v193, v99
	s_sub_i32 s59, s59, 64
	s_add_i32 s79, s79, 64
	s_and_b64 vcc, exec, s[54:55]
	s_cbranch_vccz .LBB0_1571
